# baseline (speedup 1.0000x reference)
_Z11gemm_kernelPKfPKDF16bS0_Pf:
	s_and_b32 s3, s2, 7
	s_lshl_b32 s27, s3, 1
	s_lshl_b32 s28, s3, 24
	s_lshl_b32 s29, s3, 16
	s_ashr_i32 s14, s2, 3
	s_lshl_b32 s12, s3, 6
	s_load_dwordx8 s[4:11], s[0:1], 0x0
	s_add_i32 s12, s12, s14
	s_bfe_u32 s18, s2, 0x10002
	s_lshl_b32 s2, s12, 6
	s_lshl_b32 s13, s18, 14
	s_and_b32 s2, s2, 0x3f00
	v_lshrrev_b32_e32 v52, 6, v0
	v_and_b32_e32 v50, 15, v0
	v_bfe_u32 v51, v0, 4, 2
	v_bfe_u32 v1, v0, 3, 3
	s_or_b32 s2, s2, s13
	v_lshl_or_b32 v102, v52, 2, v51
	v_lshl_or_b32 v104, v52, 3, v1
	v_lshlrev_b32_e32 v1, 4, v50
	s_lshl_b32 s15, s2, 9
	s_or_b32 s15, s15, s28
	s_waitcnt lgkmcnt(0)
	v_and_b32_e32 v238, 3, v52
	v_lshlrev_b32_e32 v238, 6, v238
	v_lshl_or_b32 v238, v51, 2, v238
	v_lshlrev_b32_e32 v238, 2, v238
	s_and_b32 s24, s12, 3
	s_lshl_b32 s24, s24, 8
	s_lshl_b32 s25, s18, 10
	s_add_u32 s24, s24, s25
	s_lshl_b32 s24, s24, 2
	s_add_u32 s24, s8, s24
	s_addc_u32 s25, s9, 0
	global_load_dwordx4 v[240:243], v238, s[24:25]
	global_load_dwordx4 v[244:247], v238, s[24:25] offset:64
	global_load_dwordx4 v[248:251], v238, s[24:25] offset:128
	global_load_dwordx4 v[252:255], v238, s[24:25] offset:192
	s_mov_b64 s[0:1], s[6:7]
	s_and_b32 s5, s5, 0xffff
	s_mov_b32 s7, 0x20000
	s_brev_b32 s6, -2
	v_lshl_or_b32 v1, v102, 9, v1
	s_or_b32 s2, s15, 0x4000
	s_lshl_b32 s14, s14, 8
	v_lshlrev_b32_e32 v103, 3, v0
	buffer_load_dwordx4 v[54:57], v1, s[4:7], s15 offen sc0 nt
	buffer_load_dwordx4 v[58:61], v1, s[4:7], s2 offen sc0 nt
	s_or_b32 s2, s15, 0x8000
	s_or_b32 s3, s15, 0xc000
	s_lshl_b32 s19, s18, 10
	s_and_b32 s20, s14, 0x300
	v_and_b32_e32 v105, 56, v103
	buffer_load_dwordx4 v[62:65], v1, s[4:7], s2 offen sc0 nt
	buffer_load_dwordx4 v[66:69], v1, s[4:7], s3 offen sc0 nt
	s_or_b32 s2, s15, 0x10000
	s_or_b32 s3, s15, 0x14000
	s_or_b32 s14, s19, s20
	v_lshlrev_b32_e32 v106, 1, v105
	buffer_load_dwordx4 v[70:73], v1, s[4:7], s2 offen sc0 nt
	buffer_load_dwordx4 v[74:77], v1, s[4:7], s3 offen sc0 nt
	s_or_b32 s2, s15, 0x18000
	s_or_b32 s3, s15, 0x1c000
	s_lshl_b32 s14, s14, 11
	s_or_b32 s26, s14, s29
	buffer_load_dwordx4 v[78:81], v1, s[4:7], s2 offen sc0 nt
	buffer_load_dwordx4 v[82:85], v1, s[4:7], s3 offen sc0 nt
	s_and_b32 s1, s1, 0xffff
	s_mov_b32 s2, s6
	s_mov_b32 s3, s7
	v_lshl_or_b32 v188, v104, 7, v106
	s_or_b32 s16, s26, 0x2000
	buffer_load_dwordx4 v[86:89], v188, s[0:3], s26 offen sc1
	buffer_load_dwordx4 v[90:93], v188, s[0:3], s16 offen sc1
	s_or_b32 s16, s26, 0x4000
	s_or_b32 s17, s26, 0x6000
	buffer_load_dwordx4 v[94:97], v188, s[0:3], s16 offen sc1
	buffer_load_dwordx4 v[98:101], v188, s[0:3], s17 offen sc1
	s_or_b32 s16, s15, 0x100
	s_or_b32 s17, s15, 0x4100
	buffer_load_dwordx4 v[10:13], v1, s[4:7], s16 offen sc0 nt
	buffer_load_dwordx4 v[18:21], v1, s[4:7], s17 offen sc0 nt
	s_or_b32 s16, s15, 0x8100
	s_or_b32 s17, s15, 0xc100
	buffer_load_dwordx4 v[22:25], v1, s[4:7], s16 offen sc0 nt
	buffer_load_dwordx4 v[30:33], v1, s[4:7], s17 offen sc0 nt
	s_or_b32 s16, s15, 0x10100
	s_or_b32 s17, s15, 0x14100
	buffer_load_dwordx4 v[34:37], v1, s[4:7], s16 offen sc0 nt
	buffer_load_dwordx4 v[38:41], v1, s[4:7], s17 offen sc0 nt
	s_or_b32 s16, s15, 0x18100
	s_or_b32 s15, s15, 0x1c100
	buffer_load_dwordx4 v[42:45], v1, s[4:7], s16 offen sc0 nt
	buffer_load_dwordx4 v[46:49], v1, s[4:7], s15 offen sc0 nt
	s_or_b32 s15, s26, 0x8000
	s_or_b32 s16, s26, 0xa000
	buffer_load_dwordx4 v[2:5], v188, s[0:3], s15 offen sc1
	buffer_load_dwordx4 v[6:9], v188, s[0:3], s16 offen sc1
	s_or_b32 s15, s26, 0xc000
	s_or_b32 s16, s26, 0xe000
	buffer_load_dwordx4 v[14:17], v188, s[0:3], s15 offen sc1
	buffer_load_dwordx4 v[26:29], v188, s[0:3], s16 offen sc1
	v_lshrrev_b32_e32 v107, 7, v0
	v_bfe_u32 v108, v0, 3, 1
	v_lshlrev_b32_e32 v102, 6, v102
	s_movk_i32 s2, 0x3c0
	v_and_or_b32 v102, v102, s2, v105
	v_lshrrev_b32_e32 v105, 2, v0
	v_and_or_b32 v107, v107, 2, v108
	v_and_b32_e32 v105, 32, v105
	v_lshlrev_b32_e32 v107, 10, v107
	v_bfe_u32 v103, v103, 5, 1
	v_lshlrev_b32_e32 v104, 6, v104
	v_and_b32_e32 v106, 48, v106
	v_bitop3_b32 v189, v102, v107, v105 bitop3:0xde
	v_and_or_b32 v103, v52, 6, v103
	v_and_or_b32 v104, v104, s2, v106
	v_lshrrev_b32_e32 v106, 1, v0
	v_lshlrev_b32_e32 v103, 10, v103
	v_and_b32_e32 v106, 32, v106
	v_bitop3_b32 v190, v104, v103, v106 bitop3:0xde
	v_lshrrev_b32_e32 v53, 8, v0
	s_movk_i32 s15, 0x4000
	s_mov_b32 s16, 0x8000
	s_mov_b32 s17, 0xc000
	s_waitcnt vmcnt(23)
	v_cvt_pk_bf16_f32 v57, v56, v57
	v_cvt_pk_bf16_f32 v56, v54, v55
	s_waitcnt vmcnt(22)
	v_cvt_pk_bf16_f32 v55, v60, v61
	v_cvt_pk_bf16_f32 v54, v58, v59
	ds_write2st64_b64 v189, v[56:57], v[54:55] offset1:8
	s_waitcnt vmcnt(21)
	v_cvt_pk_bf16_f32 v55, v64, v65
	v_cvt_pk_bf16_f32 v54, v62, v63
	s_waitcnt vmcnt(20)
	v_cvt_pk_bf16_f32 v57, v68, v69
	v_cvt_pk_bf16_f32 v56, v66, v67
	ds_write2st64_b64 v189, v[54:55], v[56:57] offset0:16 offset1:24
	s_waitcnt vmcnt(19)
	v_cvt_pk_bf16_f32 v55, v72, v73
	v_cvt_pk_bf16_f32 v54, v70, v71
	s_waitcnt vmcnt(18)
	v_cvt_pk_bf16_f32 v57, v76, v77
	v_cvt_pk_bf16_f32 v56, v74, v75
	ds_write2st64_b64 v189, v[54:55], v[56:57] offset0:32 offset1:40
	s_waitcnt vmcnt(17)
	v_cvt_pk_bf16_f32 v55, v80, v81
	v_cvt_pk_bf16_f32 v54, v78, v79
	s_waitcnt vmcnt(16)
	v_cvt_pk_bf16_f32 v57, v84, v85
	v_cvt_pk_bf16_f32 v56, v82, v83
	ds_write2st64_b64 v189, v[54:55], v[56:57] offset0:48 offset1:56
	s_waitcnt vmcnt(15)
	ds_write_b128 v190, v[86:89] offset:32768
	s_waitcnt vmcnt(14)
	ds_write_b128 v190, v[90:93] offset:40960
	s_waitcnt vmcnt(13)
	ds_write_b128 v190, v[94:97] offset:49152
	s_waitcnt vmcnt(12)
	ds_write_b128 v190, v[98:101] offset:57344
	s_waitcnt lgkmcnt(0)
	s_barrier
	v_cmp_eq_u32_e32 vcc, 1, v53
	s_and_saveexec_b64 s[2:3], vcc
	s_cbranch_execz .LBB1_2
	s_barrier

.LBB1_4:
	v_add_u32_e32 v182, s19, v191
	v_add_u32_e32 v238, s19, v192
	ds_read_b128 v[178:181], v182 offset:32768
	ds_read_b128 v[194:197], v182 offset:34816
	ds_read_b128 v[198:201], v182 offset:36864
	ds_read_b128 v[202:205], v182 offset:38912
	ds_read_b128 v[206:209], v238
	ds_read_b128 v[210:213], v238 offset:2048
	ds_read_b128 v[214:217], v238 offset:4096
	ds_read_b128 v[218:221], v238 offset:6144
	ds_read_b128 v[222:225], v238 offset:8192
	ds_read_b128 v[226:229], v238 offset:10240
	ds_read_b128 v[230:233], v238 offset:12288
	ds_read_b128 v[234:237], v238 offset:14336
	s_min_u32 s21, s20, 29
	s_xor_b32 s19, s19, 0x10000
	v_add_u32_e32 v239, s19, v189
	s_waitcnt vmcnt(11)
	v_cvt_pk_bf16_f32 v13, v12, v13
	v_cvt_pk_bf16_f32 v12, v10, v11
	s_waitcnt vmcnt(10)
	v_cvt_pk_bf16_f32 v11, v20, v21
	v_cvt_pk_bf16_f32 v10, v18, v19
	ds_write2st64_b64 v239, v[12:13], v[10:11] offset1:8
	s_waitcnt vmcnt(9)
	v_cvt_pk_bf16_f32 v11, v24, v25
	v_cvt_pk_bf16_f32 v10, v22, v23
	s_waitcnt vmcnt(8)
	v_cvt_pk_bf16_f32 v13, v32, v33
	v_cvt_pk_bf16_f32 v12, v30, v31
	ds_write2st64_b64 v239, v[10:11], v[12:13] offset0:16 offset1:24
	s_waitcnt vmcnt(7)
	v_cvt_pk_bf16_f32 v11, v36, v37
	v_cvt_pk_bf16_f32 v10, v34, v35
	s_waitcnt vmcnt(6)
	v_cvt_pk_bf16_f32 v13, v40, v41
	v_cvt_pk_bf16_f32 v12, v38, v39
	ds_write2st64_b64 v239, v[10:11], v[12:13] offset0:32 offset1:40
	s_waitcnt vmcnt(5)
	v_cvt_pk_bf16_f32 v11, v44, v45
	v_cvt_pk_bf16_f32 v10, v42, v43
	s_waitcnt vmcnt(4)
	v_cvt_pk_bf16_f32 v13, v48, v49
	v_cvt_pk_bf16_f32 v12, v46, v47
	ds_write2st64_b64 v239, v[10:11], v[12:13] offset0:48 offset1:56
	s_waitcnt lgkmcnt(0)
	s_add_i32 s21, s21, 2
	s_barrier
	s_waitcnt lgkmcnt(11)
	v_mfma_f32_16x16x32_bf16 v[174:177], v[178:181], v[206:209], v[174:177]
	s_lshl_b32 s22, s21, 1
	s_and_b32 s22, s22, 0x60
	s_add_i32 s22, s22, s12
	s_lshl_b32 s22, s22, 6
	v_mfma_f32_16x16x32_bf16 v[170:173], v[194:197], v[206:209], v[170:173]
	s_and_b32 s22, s22, 0x3f00
	s_or_b32 s22, s22, s13
	s_add_i32 s26, s21, s27
	s_lshl_b32 s23, s26, 23
	s_lshl_b32 s22, s22, 9
	v_mfma_f32_16x16x32_bf16 v[158:161], v[198:201], v[206:209], v[158:161]
	s_and_b32 s23, s23, 0x7000000
	s_or_b32 s22, s22, s23
	s_lshl_b32 s23, s21, 8
	s_and_b32 s23, s23, 0x100
	s_or_b32 s22, s22, s23
	s_or_b32 s23, s22, 0x4000
	buffer_load_dwordx4 v[10:13], v1, s[4:7], s22 offen sc0 nt
	v_mfma_f32_16x16x32_bf16 v[142:145], v[202:205], v[206:209], v[142:145]
	s_waitcnt lgkmcnt(10)
	v_mfma_f32_16x16x32_bf16 v[166:169], v[178:181], v[210:213], v[166:169]
	v_mfma_f32_16x16x32_bf16 v[162:165], v[194:197], v[210:213], v[162:165]
	v_mfma_f32_16x16x32_bf16 v[146:149], v[198:201], v[210:213], v[146:149]
	buffer_load_dwordx4 v[18:21], v1, s[4:7], s23 offen sc0 nt
	s_or_b32 s23, s22, 0x8000
	v_mfma_f32_16x16x32_bf16 v[122:125], v[202:205], v[210:213], v[122:125]
	s_waitcnt lgkmcnt(9)
	v_mfma_f32_16x16x32_bf16 v[154:157], v[178:181], v[214:217], v[154:157]
	v_mfma_f32_16x16x32_bf16 v[150:153], v[194:197], v[214:217], v[150:153]
	v_mfma_f32_16x16x32_bf16 v[130:133], v[198:201], v[214:217], v[130:133]
	buffer_load_dwordx4 v[22:25], v1, s[4:7], s23 offen sc0 nt
	s_or_b32 s23, s22, 0xc000
	v_mfma_f32_16x16x32_bf16 v[106:109], v[202:205], v[214:217], v[106:109]
	s_waitcnt lgkmcnt(8)
	v_mfma_f32_16x16x32_bf16 v[138:141], v[178:181], v[218:221], v[138:141]
	v_mfma_f32_16x16x32_bf16 v[134:137], v[194:197], v[218:221], v[134:137]
	v_mfma_f32_16x16x32_bf16 v[114:117], v[198:201], v[218:221], v[114:117]
	buffer_load_dwordx4 v[30:33], v1, s[4:7], s23 offen sc0 nt
	s_or_b32 s23, s22, 0x10000
	v_mfma_f32_16x16x32_bf16 v[90:93], v[202:205], v[218:221], v[90:93]
	s_waitcnt lgkmcnt(7)
	v_mfma_f32_16x16x32_bf16 v[126:129], v[178:181], v[222:225], v[126:129]
	v_mfma_f32_16x16x32_bf16 v[118:121], v[194:197], v[222:225], v[118:121]
	v_mfma_f32_16x16x32_bf16 v[98:101], v[198:201], v[222:225], v[98:101]
	buffer_load_dwordx4 v[34:37], v1, s[4:7], s23 offen sc0 nt
	s_or_b32 s23, s22, 0x14000
	v_mfma_f32_16x16x32_bf16 v[74:77], v[202:205], v[222:225], v[74:77]
	s_waitcnt lgkmcnt(6)
	v_mfma_f32_16x16x32_bf16 v[110:113], v[178:181], v[226:229], v[110:113]
	v_mfma_f32_16x16x32_bf16 v[102:105], v[194:197], v[226:229], v[102:105]
	v_mfma_f32_16x16x32_bf16 v[82:85], v[198:201], v[226:229], v[82:85]
	buffer_load_dwordx4 v[38:41], v1, s[4:7], s23 offen sc0 nt
	s_or_b32 s23, s22, 0x18000
	s_or_b32 s22, s22, 0x1c000
	v_mfma_f32_16x16x32_bf16 v[62:65], v[202:205], v[226:229], v[62:65]
	s_waitcnt lgkmcnt(5)
	v_mfma_f32_16x16x32_bf16 v[94:97], v[178:181], v[230:233], v[94:97]
	v_mfma_f32_16x16x32_bf16 v[86:89], v[194:197], v[230:233], v[86:89]
	v_mfma_f32_16x16x32_bf16 v[70:73], v[198:201], v[230:233], v[70:73]
	buffer_load_dwordx4 v[42:45], v1, s[4:7], s23 offen sc0 nt
	v_mfma_f32_16x16x32_bf16 v[54:57], v[202:205], v[230:233], v[54:57]
	s_waitcnt lgkmcnt(4)
	v_mfma_f32_16x16x32_bf16 v[78:81], v[178:181], v[234:237], v[78:81]
	v_mfma_f32_16x16x32_bf16 v[66:69], v[194:197], v[234:237], v[66:69]
	v_mfma_f32_16x16x32_bf16 v[58:61], v[198:201], v[234:237], v[58:61]
	buffer_load_dwordx4 v[46:49], v1, s[4:7], s22 offen sc0 nt
	v_mfma_f32_16x16x32_bf16 v[50:53], v[202:205], v[234:237], v[50:53]
	s_waitcnt lgkmcnt(0)
	s_barrier
	ds_read_b128 v[178:181], v182 offset:33792
	ds_read_b128 v[194:197], v182 offset:35840
	ds_read_b128 v[198:201], v182 offset:37888
	ds_read_b128 v[202:205], v182 offset:39936
	ds_read_b128 v[206:209], v238 offset:1024
	ds_read_b128 v[210:213], v238 offset:3072
	ds_read_b128 v[214:217], v238 offset:5120
	ds_read_b128 v[218:221], v238 offset:7168
	ds_read_b128 v[222:225], v238 offset:9216
	ds_read_b128 v[226:229], v238 offset:11264
	ds_read_b128 v[230:233], v238 offset:13312
	ds_read_b128 v[234:237], v238 offset:15360
	v_add_u32_e32 v182, s19, v190
	s_waitcnt vmcnt(11)
	ds_write_b128 v182, v[2:5] offset:32768
	s_waitcnt vmcnt(10)
	ds_write_b128 v182, v[6:9] offset:40960
	s_waitcnt vmcnt(9)
	ds_write_b128 v182, v[14:17] offset:49152
	s_waitcnt vmcnt(8)
	ds_write_b128 v182, v[26:29] offset:57344
	s_waitcnt lgkmcnt(0)
	s_barrier
	s_waitcnt lgkmcnt(11)
	v_mfma_f32_16x16x32_bf16 v[174:177], v[178:181], v[206:209], v[174:177]
	s_lshl_b32 s21, s26, 15
	s_and_b32 s21, s21, 0x78000
	s_or_b32 s21, s21, s14
	s_or_b32 s22, s21, 0x2000
	v_mfma_f32_16x16x32_bf16 v[170:173], v[194:197], v[206:209], v[170:173]
	v_mfma_f32_16x16x32_bf16 v[158:161], v[198:201], v[206:209], v[158:161]
	v_mfma_f32_16x16x32_bf16 v[142:145], v[202:205], v[206:209], v[142:145]
	s_waitcnt lgkmcnt(10)
	v_mfma_f32_16x16x32_bf16 v[166:169], v[178:181], v[210:213], v[166:169]
	v_mfma_f32_16x16x32_bf16 v[162:165], v[194:197], v[210:213], v[162:165]
	buffer_load_dwordx4 v[2:5], v188, s[0:3], s21 offen sc1
	v_mfma_f32_16x16x32_bf16 v[146:149], v[198:201], v[210:213], v[146:149]
	v_mfma_f32_16x16x32_bf16 v[122:125], v[202:205], v[210:213], v[122:125]
	s_waitcnt lgkmcnt(9)
	v_mfma_f32_16x16x32_bf16 v[154:157], v[178:181], v[214:217], v[154:157]
	v_mfma_f32_16x16x32_bf16 v[150:153], v[194:197], v[214:217], v[150:153]
	v_mfma_f32_16x16x32_bf16 v[130:133], v[198:201], v[214:217], v[130:133]
	v_mfma_f32_16x16x32_bf16 v[106:109], v[202:205], v[214:217], v[106:109]
	s_waitcnt lgkmcnt(8)
	v_mfma_f32_16x16x32_bf16 v[138:141], v[178:181], v[218:221], v[138:141]
	v_mfma_f32_16x16x32_bf16 v[134:137], v[194:197], v[218:221], v[134:137]
	buffer_load_dwordx4 v[6:9], v188, s[0:3], s22 offen sc1
	s_or_b32 s22, s21, 0x4000
	s_or_b32 s21, s21, 0x6000
	v_mfma_f32_16x16x32_bf16 v[114:117], v[198:201], v[218:221], v[114:117]
	v_mfma_f32_16x16x32_bf16 v[90:93], v[202:205], v[218:221], v[90:93]
	s_waitcnt lgkmcnt(7)
	v_mfma_f32_16x16x32_bf16 v[126:129], v[178:181], v[222:225], v[126:129]
	v_mfma_f32_16x16x32_bf16 v[118:121], v[194:197], v[222:225], v[118:121]
	v_mfma_f32_16x16x32_bf16 v[98:101], v[198:201], v[222:225], v[98:101]
	v_mfma_f32_16x16x32_bf16 v[74:77], v[202:205], v[222:225], v[74:77]
	s_waitcnt lgkmcnt(6)
	v_mfma_f32_16x16x32_bf16 v[110:113], v[178:181], v[226:229], v[110:113]
	v_mfma_f32_16x16x32_bf16 v[102:105], v[194:197], v[226:229], v[102:105]
	buffer_load_dwordx4 v[14:17], v188, s[0:3], s22 offen sc1
	v_mfma_f32_16x16x32_bf16 v[82:85], v[198:201], v[226:229], v[82:85]
	v_mfma_f32_16x16x32_bf16 v[62:65], v[202:205], v[226:229], v[62:65]
	s_waitcnt lgkmcnt(5)
	v_mfma_f32_16x16x32_bf16 v[94:97], v[178:181], v[230:233], v[94:97]
	v_mfma_f32_16x16x32_bf16 v[86:89], v[194:197], v[230:233], v[86:89]
	v_mfma_f32_16x16x32_bf16 v[70:73], v[198:201], v[230:233], v[70:73]
	v_mfma_f32_16x16x32_bf16 v[54:57], v[202:205], v[230:233], v[54:57]
	s_waitcnt lgkmcnt(4)
	v_mfma_f32_16x16x32_bf16 v[78:81], v[178:181], v[234:237], v[78:81]
	v_mfma_f32_16x16x32_bf16 v[66:69], v[194:197], v[234:237], v[66:69]
	buffer_load_dwordx4 v[26:29], v188, s[0:3], s21 offen sc1
	v_mfma_f32_16x16x32_bf16 v[58:61], v[198:201], v[234:237], v[58:61]
	v_mfma_f32_16x16x32_bf16 v[50:53], v[202:205], v[234:237], v[50:53]
	s_and_b32 s21, s20, 15
	s_cmp_lg_u32 s21, 15
	s_cbranch_scc1 .LBB1_3
	s_and_b32 s21, s18, 32
	s_add_i32 s21, s21, s12
	s_lshl_b32 s21, s21, 6
	s_and_b32 s21, s21, 0x3f00
	v_add_lshl_u32 v182, v193, s21, 9
	v_lshl_add_u64 v[206:207], v[184:185], 0, v[182:183]
	v_add_co_u32_e32 v208, vcc, s8, v206
	s_nop 1
	v_addc_co_u32_e32 v209, vcc, 0, v207, vcc
	v_add_co_u32_e32 v210, vcc, s15, v206
	s_nop 1
	v_addc_co_u32_e32 v211, vcc, 0, v207, vcc
	v_add_co_u32_e32 v212, vcc, s9, v206
	s_nop 1
	v_addc_co_u32_e32 v213, vcc, 0, v207, vcc
	v_add_co_u32_e32 v214, vcc, s16, v206
	s_nop 1
	v_addc_co_u32_e32 v215, vcc, 0, v207, vcc
	v_add_co_u32_e32 v216, vcc, s10, v206
	s_nop 1
	v_addc_co_u32_e32 v217, vcc, 0, v207, vcc
	v_add_co_u32_e32 v218, vcc, s17, v206
	s_nop 1
	v_addc_co_u32_e32 v219, vcc, 0, v207, vcc
	v_add_co_u32_e32 v220, vcc, s11, v206
	s_nop 1
	v_addc_co_u32_e32 v221, vcc, 0, v207, vcc
	global_store_dwordx4 v[206:207], v[174:177], off
	global_store_dwordx4 v[206:207], v[170:173], off offset:64
	global_store_dwordx4 v[206:207], v[158:161], off offset:128
	global_store_dwordx4 v[206:207], v[142:145], off offset:192
	global_store_dwordx4 v[208:209], v[166:169], off
	global_store_dwordx4 v[208:209], v[162:165], off offset:64
	global_store_dwordx4 v[208:209], v[146:149], off offset:128
	global_store_dwordx4 v[208:209], v[122:125], off offset:192
	global_store_dwordx4 v[210:211], v[154:157], off
	global_store_dwordx4 v[210:211], v[150:153], off offset:64
	global_store_dwordx4 v[210:211], v[130:133], off offset:128
	global_store_dwordx4 v[210:211], v[106:109], off offset:192
	global_store_dwordx4 v[212:213], v[138:141], off
	global_store_dwordx4 v[212:213], v[134:137], off offset:64
	global_store_dwordx4 v[212:213], v[114:117], off offset:128
	global_store_dwordx4 v[212:213], v[90:93], off offset:192
	global_store_dwordx4 v[214:215], v[126:129], off
	global_store_dwordx4 v[214:215], v[118:121], off offset:64
	global_store_dwordx4 v[214:215], v[98:101], off offset:128
	global_store_dwordx4 v[214:215], v[74:77], off offset:192
	global_store_dwordx4 v[216:217], v[110:113], off
	global_store_dwordx4 v[216:217], v[102:105], off offset:64
	global_store_dwordx4 v[216:217], v[82:85], off offset:128
	global_store_dwordx4 v[216:217], v[62:65], off offset:192
	global_store_dwordx4 v[218:219], v[94:97], off
	global_store_dwordx4 v[218:219], v[86:89], off offset:64
	global_store_dwordx4 v[218:219], v[70:73], off offset:128
	global_store_dwordx4 v[218:219], v[54:57], off offset:192
	global_store_dwordx4 v[220:221], v[78:81], off
	global_store_dwordx4 v[220:221], v[66:69], off offset:64
	global_store_dwordx4 v[220:221], v[58:61], off offset:128
	global_store_dwordx4 v[220:221], v[50:53], off offset:192
.Lpd_tail:
	s_waitcnt lgkmcnt(0)
	s_barrier
	s_add_i32 s20, s20, 1
	s_add_i32 s18, s18, 2
	v_add_u32_e32 v182, s19, v191
	v_add_u32_e32 v238, s19, v192
	ds_read_b128 v[178:181], v182 offset:32768
	ds_read_b128 v[194:197], v182 offset:34816
	ds_read_b128 v[198:201], v182 offset:36864
	ds_read_b128 v[202:205], v182 offset:38912
	ds_read_b128 v[206:209], v238
	ds_read_b128 v[210:213], v238 offset:2048
	ds_read_b128 v[214:217], v238 offset:4096
	ds_read_b128 v[218:221], v238 offset:6144
	ds_read_b128 v[222:225], v238 offset:8192
	ds_read_b128 v[226:229], v238 offset:10240
	ds_read_b128 v[230:233], v238 offset:12288
	ds_read_b128 v[234:237], v238 offset:14336
	s_min_u32 s21, s20, 29
	s_xor_b32 s19, s19, 0x10000
	v_add_u32_e32 v239, s19, v189
	s_waitcnt vmcnt(43)
	v_cvt_pk_bf16_f32 v13, v12, v13
	v_cvt_pk_bf16_f32 v12, v10, v11
	s_waitcnt vmcnt(42)
	v_cvt_pk_bf16_f32 v11, v20, v21
	v_cvt_pk_bf16_f32 v10, v18, v19
	ds_write2st64_b64 v239, v[12:13], v[10:11] offset1:8
	s_waitcnt vmcnt(41)
	v_cvt_pk_bf16_f32 v11, v24, v25
	v_cvt_pk_bf16_f32 v10, v22, v23
	s_waitcnt vmcnt(40)
	v_cvt_pk_bf16_f32 v13, v32, v33
	v_cvt_pk_bf16_f32 v12, v30, v31
	ds_write2st64_b64 v239, v[10:11], v[12:13] offset0:16 offset1:24
	s_waitcnt vmcnt(39)
	v_cvt_pk_bf16_f32 v11, v36, v37
	v_cvt_pk_bf16_f32 v10, v34, v35
	s_waitcnt vmcnt(38)
	v_cvt_pk_bf16_f32 v13, v40, v41
	v_cvt_pk_bf16_f32 v12, v38, v39
	ds_write2st64_b64 v239, v[10:11], v[12:13] offset0:32 offset1:40
	s_waitcnt vmcnt(37)
	v_cvt_pk_bf16_f32 v11, v44, v45
	v_cvt_pk_bf16_f32 v10, v42, v43
	s_waitcnt vmcnt(36)
	v_cvt_pk_bf16_f32 v13, v48, v49
	v_cvt_pk_bf16_f32 v12, v46, v47
	ds_write2st64_b64 v239, v[10:11], v[12:13] offset0:48 offset1:56
	s_waitcnt lgkmcnt(0)
	s_add_i32 s21, s21, 2
	s_barrier
	s_waitcnt lgkmcnt(11)
	v_mfma_f32_16x16x32_bf16 v[174:177], v[178:181], v[206:209], v[240:243]
	s_lshl_b32 s22, s21, 1
	s_and_b32 s22, s22, 0x60
	s_add_i32 s22, s22, s12
	s_lshl_b32 s22, s22, 6
	v_mfma_f32_16x16x32_bf16 v[170:173], v[194:197], v[206:209], v[244:247]
	s_and_b32 s22, s22, 0x3f00
	s_or_b32 s22, s22, s13
	s_add_i32 s26, s21, s27
	s_lshl_b32 s23, s26, 23
	s_lshl_b32 s22, s22, 9
	v_mfma_f32_16x16x32_bf16 v[158:161], v[198:201], v[206:209], v[248:251]
	s_and_b32 s23, s23, 0x7000000
	s_or_b32 s22, s22, s23
	s_lshl_b32 s23, s21, 8
	s_and_b32 s23, s23, 0x100
	s_or_b32 s22, s22, s23
	s_or_b32 s23, s22, 0x4000
	buffer_load_dwordx4 v[10:13], v1, s[4:7], s22 offen sc0 nt
	v_mfma_f32_16x16x32_bf16 v[142:145], v[202:205], v[206:209], v[252:255]
	s_waitcnt lgkmcnt(10)
	v_mfma_f32_16x16x32_bf16 v[166:169], v[178:181], v[210:213], v[240:243]
	v_mfma_f32_16x16x32_bf16 v[162:165], v[194:197], v[210:213], v[244:247]
	v_mfma_f32_16x16x32_bf16 v[146:149], v[198:201], v[210:213], v[248:251]
	buffer_load_dwordx4 v[18:21], v1, s[4:7], s23 offen sc0 nt
	s_or_b32 s23, s22, 0x8000
	v_mfma_f32_16x16x32_bf16 v[122:125], v[202:205], v[210:213], v[252:255]
	s_waitcnt lgkmcnt(9)
	v_mfma_f32_16x16x32_bf16 v[154:157], v[178:181], v[214:217], v[240:243]
	v_mfma_f32_16x16x32_bf16 v[150:153], v[194:197], v[214:217], v[244:247]
	v_mfma_f32_16x16x32_bf16 v[130:133], v[198:201], v[214:217], v[248:251]
	buffer_load_dwordx4 v[22:25], v1, s[4:7], s23 offen sc0 nt
	s_or_b32 s23, s22, 0xc000
	v_mfma_f32_16x16x32_bf16 v[106:109], v[202:205], v[214:217], v[252:255]
	s_waitcnt lgkmcnt(8)
	v_mfma_f32_16x16x32_bf16 v[138:141], v[178:181], v[218:221], v[240:243]
	v_mfma_f32_16x16x32_bf16 v[134:137], v[194:197], v[218:221], v[244:247]
	v_mfma_f32_16x16x32_bf16 v[114:117], v[198:201], v[218:221], v[248:251]
	buffer_load_dwordx4 v[30:33], v1, s[4:7], s23 offen sc0 nt
	s_or_b32 s23, s22, 0x10000
	v_mfma_f32_16x16x32_bf16 v[90:93], v[202:205], v[218:221], v[252:255]
	s_waitcnt lgkmcnt(7)
	v_mfma_f32_16x16x32_bf16 v[126:129], v[178:181], v[222:225], v[240:243]
	v_mfma_f32_16x16x32_bf16 v[118:121], v[194:197], v[222:225], v[244:247]
	v_mfma_f32_16x16x32_bf16 v[98:101], v[198:201], v[222:225], v[248:251]
	buffer_load_dwordx4 v[34:37], v1, s[4:7], s23 offen sc0 nt
	s_or_b32 s23, s22, 0x14000
	v_mfma_f32_16x16x32_bf16 v[74:77], v[202:205], v[222:225], v[252:255]
	s_waitcnt lgkmcnt(6)
	v_mfma_f32_16x16x32_bf16 v[110:113], v[178:181], v[226:229], v[240:243]
	v_mfma_f32_16x16x32_bf16 v[102:105], v[194:197], v[226:229], v[244:247]
	v_mfma_f32_16x16x32_bf16 v[82:85], v[198:201], v[226:229], v[248:251]
	buffer_load_dwordx4 v[38:41], v1, s[4:7], s23 offen sc0 nt
	s_or_b32 s23, s22, 0x18000
	s_or_b32 s22, s22, 0x1c000
	v_mfma_f32_16x16x32_bf16 v[62:65], v[202:205], v[226:229], v[252:255]
	s_waitcnt lgkmcnt(5)
	v_mfma_f32_16x16x32_bf16 v[94:97], v[178:181], v[230:233], v[240:243]
	v_mfma_f32_16x16x32_bf16 v[86:89], v[194:197], v[230:233], v[244:247]
	v_mfma_f32_16x16x32_bf16 v[70:73], v[198:201], v[230:233], v[248:251]
	buffer_load_dwordx4 v[42:45], v1, s[4:7], s23 offen sc0 nt
	v_mfma_f32_16x16x32_bf16 v[54:57], v[202:205], v[230:233], v[252:255]
	s_waitcnt lgkmcnt(4)
	v_mfma_f32_16x16x32_bf16 v[78:81], v[178:181], v[234:237], v[240:243]
	v_mfma_f32_16x16x32_bf16 v[66:69], v[194:197], v[234:237], v[244:247]
	v_mfma_f32_16x16x32_bf16 v[58:61], v[198:201], v[234:237], v[248:251]
	buffer_load_dwordx4 v[46:49], v1, s[4:7], s22 offen sc0 nt
	v_mfma_f32_16x16x32_bf16 v[50:53], v[202:205], v[234:237], v[252:255]
	s_waitcnt lgkmcnt(0)
	s_barrier
	ds_read_b128 v[178:181], v182 offset:33792
	ds_read_b128 v[194:197], v182 offset:35840
	ds_read_b128 v[198:201], v182 offset:37888
	ds_read_b128 v[202:205], v182 offset:39936
	ds_read_b128 v[206:209], v238 offset:1024
	ds_read_b128 v[210:213], v238 offset:3072
	ds_read_b128 v[214:217], v238 offset:5120
	ds_read_b128 v[218:221], v238 offset:7168
	ds_read_b128 v[222:225], v238 offset:9216
	ds_read_b128 v[226:229], v238 offset:11264
	ds_read_b128 v[230:233], v238 offset:13312
	ds_read_b128 v[234:237], v238 offset:15360
	v_add_u32_e32 v182, s19, v190
	s_waitcnt vmcnt(43)
	ds_write_b128 v182, v[2:5] offset:32768
	s_waitcnt vmcnt(42)
	ds_write_b128 v182, v[6:9] offset:40960
	s_waitcnt vmcnt(41)
	ds_write_b128 v182, v[14:17] offset:49152
	s_waitcnt vmcnt(40)
	ds_write_b128 v182, v[26:29] offset:57344
	s_waitcnt lgkmcnt(0)
	s_barrier
	s_waitcnt lgkmcnt(11)
	v_mfma_f32_16x16x32_bf16 v[174:177], v[178:181], v[206:209], v[174:177]
	s_lshl_b32 s21, s26, 15
	s_and_b32 s21, s21, 0x78000
	s_or_b32 s21, s21, s14
	s_or_b32 s22, s21, 0x2000
	v_mfma_f32_16x16x32_bf16 v[170:173], v[194:197], v[206:209], v[170:173]
	v_mfma_f32_16x16x32_bf16 v[158:161], v[198:201], v[206:209], v[158:161]
	v_mfma_f32_16x16x32_bf16 v[142:145], v[202:205], v[206:209], v[142:145]
	s_waitcnt lgkmcnt(10)
	v_mfma_f32_16x16x32_bf16 v[166:169], v[178:181], v[210:213], v[166:169]
	v_mfma_f32_16x16x32_bf16 v[162:165], v[194:197], v[210:213], v[162:165]
	buffer_load_dwordx4 v[2:5], v188, s[0:3], s21 offen sc1
	v_mfma_f32_16x16x32_bf16 v[146:149], v[198:201], v[210:213], v[146:149]
	v_mfma_f32_16x16x32_bf16 v[122:125], v[202:205], v[210:213], v[122:125]
	s_waitcnt lgkmcnt(9)
	v_mfma_f32_16x16x32_bf16 v[154:157], v[178:181], v[214:217], v[154:157]
	v_mfma_f32_16x16x32_bf16 v[150:153], v[194:197], v[214:217], v[150:153]
	v_mfma_f32_16x16x32_bf16 v[130:133], v[198:201], v[214:217], v[130:133]
	v_mfma_f32_16x16x32_bf16 v[106:109], v[202:205], v[214:217], v[106:109]
	s_waitcnt lgkmcnt(8)
	v_mfma_f32_16x16x32_bf16 v[138:141], v[178:181], v[218:221], v[138:141]
	v_mfma_f32_16x16x32_bf16 v[134:137], v[194:197], v[218:221], v[134:137]
	buffer_load_dwordx4 v[6:9], v188, s[0:3], s22 offen sc1
	s_or_b32 s22, s21, 0x4000
	s_or_b32 s21, s21, 0x6000
	v_mfma_f32_16x16x32_bf16 v[114:117], v[198:201], v[218:221], v[114:117]
	v_mfma_f32_16x16x32_bf16 v[90:93], v[202:205], v[218:221], v[90:93]
	s_waitcnt lgkmcnt(7)
	v_mfma_f32_16x16x32_bf16 v[126:129], v[178:181], v[222:225], v[126:129]
	v_mfma_f32_16x16x32_bf16 v[118:121], v[194:197], v[222:225], v[118:121]
	v_mfma_f32_16x16x32_bf16 v[98:101], v[198:201], v[222:225], v[98:101]
	v_mfma_f32_16x16x32_bf16 v[74:77], v[202:205], v[222:225], v[74:77]
	s_waitcnt lgkmcnt(6)
	v_mfma_f32_16x16x32_bf16 v[110:113], v[178:181], v[226:229], v[110:113]
	v_mfma_f32_16x16x32_bf16 v[102:105], v[194:197], v[226:229], v[102:105]
	buffer_load_dwordx4 v[14:17], v188, s[0:3], s22 offen sc1
	v_mfma_f32_16x16x32_bf16 v[82:85], v[198:201], v[226:229], v[82:85]
	v_mfma_f32_16x16x32_bf16 v[62:65], v[202:205], v[226:229], v[62:65]
	s_waitcnt lgkmcnt(5)
	v_mfma_f32_16x16x32_bf16 v[94:97], v[178:181], v[230:233], v[94:97]
	v_mfma_f32_16x16x32_bf16 v[86:89], v[194:197], v[230:233], v[86:89]
	v_mfma_f32_16x16x32_bf16 v[70:73], v[198:201], v[230:233], v[70:73]
	v_mfma_f32_16x16x32_bf16 v[54:57], v[202:205], v[230:233], v[54:57]
	s_waitcnt lgkmcnt(4)
	v_mfma_f32_16x16x32_bf16 v[78:81], v[178:181], v[234:237], v[78:81]
	v_mfma_f32_16x16x32_bf16 v[66:69], v[194:197], v[234:237], v[66:69]
	buffer_load_dwordx4 v[26:29], v188, s[0:3], s21 offen sc1
	v_mfma_f32_16x16x32_bf16 v[58:61], v[198:201], v[234:237], v[58:61]
	v_mfma_f32_16x16x32_bf16 v[50:53], v[202:205], v[234:237], v[50:53]
	s_branch .LBB1_3
.Lt30:
	v_add_u32_e32 v182, s19, v191
	v_add_u32_e32 v238, s19, v192
	ds_read_b128 v[178:181], v182 offset:32768
	ds_read_b128 v[194:197], v182 offset:34816
	ds_read_b128 v[198:201], v182 offset:36864
	ds_read_b128 v[202:205], v182 offset:38912
	ds_read_b128 v[206:209], v238
	ds_read_b128 v[210:213], v238 offset:2048
	ds_read_b128 v[214:217], v238 offset:4096
	ds_read_b128 v[218:221], v238 offset:6144
	ds_read_b128 v[222:225], v238 offset:8192
	ds_read_b128 v[226:229], v238 offset:10240
	ds_read_b128 v[230:233], v238 offset:12288
	ds_read_b128 v[234:237], v238 offset:14336
	s_min_u32 s21, s20, 29
	s_xor_b32 s19, s19, 0x10000
	v_add_u32_e32 v239, s19, v189
	s_waitcnt vmcnt(11)
	v_cvt_pk_bf16_f32 v13, v12, v13
	v_cvt_pk_bf16_f32 v12, v10, v11
	s_waitcnt vmcnt(10)
	v_cvt_pk_bf16_f32 v11, v20, v21
	v_cvt_pk_bf16_f32 v10, v18, v19
	ds_write2st64_b64 v239, v[12:13], v[10:11] offset1:8
	s_waitcnt vmcnt(9)
	v_cvt_pk_bf16_f32 v11, v24, v25
	v_cvt_pk_bf16_f32 v10, v22, v23
	s_waitcnt vmcnt(8)
	v_cvt_pk_bf16_f32 v13, v32, v33
	v_cvt_pk_bf16_f32 v12, v30, v31
	ds_write2st64_b64 v239, v[10:11], v[12:13] offset0:16 offset1:24
	s_waitcnt vmcnt(7)
	v_cvt_pk_bf16_f32 v11, v36, v37
	v_cvt_pk_bf16_f32 v10, v34, v35
	s_waitcnt vmcnt(6)
	v_cvt_pk_bf16_f32 v13, v40, v41
	v_cvt_pk_bf16_f32 v12, v38, v39
	ds_write2st64_b64 v239, v[10:11], v[12:13] offset0:32 offset1:40
	s_waitcnt vmcnt(5)
	v_cvt_pk_bf16_f32 v11, v44, v45
	v_cvt_pk_bf16_f32 v10, v42, v43
	s_waitcnt vmcnt(4)
	v_cvt_pk_bf16_f32 v13, v48, v49
	v_cvt_pk_bf16_f32 v12, v46, v47
	ds_write2st64_b64 v239, v[10:11], v[12:13] offset0:48 offset1:56
	s_waitcnt lgkmcnt(0)
	s_add_i32 s21, s21, 2
	s_barrier
	s_waitcnt lgkmcnt(11)
	v_mfma_f32_16x16x32_bf16 v[174:177], v[178:181], v[206:209], v[174:177]
	s_lshl_b32 s22, s21, 1
	s_and_b32 s22, s22, 0x60
	s_add_i32 s22, s22, s12
	s_lshl_b32 s22, s22, 6
	v_mfma_f32_16x16x32_bf16 v[170:173], v[194:197], v[206:209], v[170:173]
	s_and_b32 s22, s22, 0x3f00
	s_or_b32 s22, s22, s13
	s_add_i32 s26, s21, s27
	s_lshl_b32 s23, s26, 23
	s_lshl_b32 s22, s22, 9
	v_mfma_f32_16x16x32_bf16 v[158:161], v[198:201], v[206:209], v[158:161]
	s_and_b32 s23, s23, 0x7000000
	s_or_b32 s22, s22, s23
	s_lshl_b32 s23, s21, 8
	s_and_b32 s23, s23, 0x100
	s_or_b32 s22, s22, s23
	s_or_b32 s23, s22, 0x4000
	v_mfma_f32_16x16x32_bf16 v[142:145], v[202:205], v[206:209], v[142:145]
	s_waitcnt lgkmcnt(10)
	v_mfma_f32_16x16x32_bf16 v[166:169], v[178:181], v[210:213], v[166:169]
	v_mfma_f32_16x16x32_bf16 v[162:165], v[194:197], v[210:213], v[162:165]
	v_mfma_f32_16x16x32_bf16 v[146:149], v[198:201], v[210:213], v[146:149]
	s_or_b32 s23, s22, 0x8000
	v_mfma_f32_16x16x32_bf16 v[122:125], v[202:205], v[210:213], v[122:125]
	s_waitcnt lgkmcnt(9)
	v_mfma_f32_16x16x32_bf16 v[154:157], v[178:181], v[214:217], v[154:157]
	v_mfma_f32_16x16x32_bf16 v[150:153], v[194:197], v[214:217], v[150:153]
	v_mfma_f32_16x16x32_bf16 v[130:133], v[198:201], v[214:217], v[130:133]
	s_or_b32 s23, s22, 0xc000
	v_mfma_f32_16x16x32_bf16 v[106:109], v[202:205], v[214:217], v[106:109]
	s_waitcnt lgkmcnt(8)
	v_mfma_f32_16x16x32_bf16 v[138:141], v[178:181], v[218:221], v[138:141]
	v_mfma_f32_16x16x32_bf16 v[134:137], v[194:197], v[218:221], v[134:137]
	v_mfma_f32_16x16x32_bf16 v[114:117], v[198:201], v[218:221], v[114:117]
	s_or_b32 s23, s22, 0x10000
	v_mfma_f32_16x16x32_bf16 v[90:93], v[202:205], v[218:221], v[90:93]
	s_waitcnt lgkmcnt(7)
	v_mfma_f32_16x16x32_bf16 v[126:129], v[178:181], v[222:225], v[126:129]
	v_mfma_f32_16x16x32_bf16 v[118:121], v[194:197], v[222:225], v[118:121]
	v_mfma_f32_16x16x32_bf16 v[98:101], v[198:201], v[222:225], v[98:101]
	s_or_b32 s23, s22, 0x14000
	v_mfma_f32_16x16x32_bf16 v[74:77], v[202:205], v[222:225], v[74:77]
	s_waitcnt lgkmcnt(6)
	v_mfma_f32_16x16x32_bf16 v[110:113], v[178:181], v[226:229], v[110:113]
	v_mfma_f32_16x16x32_bf16 v[102:105], v[194:197], v[226:229], v[102:105]
	v_mfma_f32_16x16x32_bf16 v[82:85], v[198:201], v[226:229], v[82:85]
	s_or_b32 s23, s22, 0x18000
	s_or_b32 s22, s22, 0x1c000
	v_mfma_f32_16x16x32_bf16 v[62:65], v[202:205], v[226:229], v[62:65]
	s_waitcnt lgkmcnt(5)
	v_mfma_f32_16x16x32_bf16 v[94:97], v[178:181], v[230:233], v[94:97]
	v_mfma_f32_16x16x32_bf16 v[86:89], v[194:197], v[230:233], v[86:89]
	v_mfma_f32_16x16x32_bf16 v[70:73], v[198:201], v[230:233], v[70:73]
	v_mfma_f32_16x16x32_bf16 v[54:57], v[202:205], v[230:233], v[54:57]
	s_waitcnt lgkmcnt(4)
	v_mfma_f32_16x16x32_bf16 v[78:81], v[178:181], v[234:237], v[78:81]
	v_mfma_f32_16x16x32_bf16 v[66:69], v[194:197], v[234:237], v[66:69]
	v_mfma_f32_16x16x32_bf16 v[58:61], v[198:201], v[234:237], v[58:61]
	v_mfma_f32_16x16x32_bf16 v[50:53], v[202:205], v[234:237], v[50:53]
	s_waitcnt lgkmcnt(0)
	s_barrier
	ds_read_b128 v[178:181], v182 offset:33792
	ds_read_b128 v[194:197], v182 offset:35840
	ds_read_b128 v[198:201], v182 offset:37888
	ds_read_b128 v[202:205], v182 offset:39936
	ds_read_b128 v[206:209], v238 offset:1024
	ds_read_b128 v[210:213], v238 offset:3072
	ds_read_b128 v[214:217], v238 offset:5120
	ds_read_b128 v[218:221], v238 offset:7168
	ds_read_b128 v[222:225], v238 offset:9216
	ds_read_b128 v[226:229], v238 offset:11264
	ds_read_b128 v[230:233], v238 offset:13312
	ds_read_b128 v[234:237], v238 offset:15360
	v_add_u32_e32 v182, s19, v190
	s_waitcnt vmcnt(3)
	ds_write_b128 v182, v[2:5] offset:32768
	s_waitcnt vmcnt(2)
	ds_write_b128 v182, v[6:9] offset:40960
	s_waitcnt vmcnt(1)
	ds_write_b128 v182, v[14:17] offset:49152
	s_waitcnt vmcnt(0)
	ds_write_b128 v182, v[26:29] offset:57344
	s_waitcnt lgkmcnt(0)
	s_barrier
	s_waitcnt lgkmcnt(11)
	v_mfma_f32_16x16x32_bf16 v[174:177], v[178:181], v[206:209], v[174:177]
	s_lshl_b32 s21, s26, 15
	s_and_b32 s21, s21, 0x78000
	s_or_b32 s21, s21, s14
	s_or_b32 s22, s21, 0x2000
	v_mfma_f32_16x16x32_bf16 v[170:173], v[194:197], v[206:209], v[170:173]
	v_mfma_f32_16x16x32_bf16 v[158:161], v[198:201], v[206:209], v[158:161]
	v_mfma_f32_16x16x32_bf16 v[142:145], v[202:205], v[206:209], v[142:145]
	s_waitcnt lgkmcnt(10)
	v_mfma_f32_16x16x32_bf16 v[166:169], v[178:181], v[210:213], v[166:169]
	v_mfma_f32_16x16x32_bf16 v[162:165], v[194:197], v[210:213], v[162:165]
	v_mfma_f32_16x16x32_bf16 v[146:149], v[198:201], v[210:213], v[146:149]
	v_mfma_f32_16x16x32_bf16 v[122:125], v[202:205], v[210:213], v[122:125]
	s_waitcnt lgkmcnt(9)
	v_mfma_f32_16x16x32_bf16 v[154:157], v[178:181], v[214:217], v[154:157]
	v_mfma_f32_16x16x32_bf16 v[150:153], v[194:197], v[214:217], v[150:153]
	v_mfma_f32_16x16x32_bf16 v[130:133], v[198:201], v[214:217], v[130:133]
	v_mfma_f32_16x16x32_bf16 v[106:109], v[202:205], v[214:217], v[106:109]
	s_waitcnt lgkmcnt(8)
	v_mfma_f32_16x16x32_bf16 v[138:141], v[178:181], v[218:221], v[138:141]
	v_mfma_f32_16x16x32_bf16 v[134:137], v[194:197], v[218:221], v[134:137]
	s_or_b32 s22, s21, 0x4000
	s_or_b32 s21, s21, 0x6000
	v_mfma_f32_16x16x32_bf16 v[114:117], v[198:201], v[218:221], v[114:117]
	v_mfma_f32_16x16x32_bf16 v[90:93], v[202:205], v[218:221], v[90:93]
	s_waitcnt lgkmcnt(7)
	v_mfma_f32_16x16x32_bf16 v[126:129], v[178:181], v[222:225], v[126:129]
	v_mfma_f32_16x16x32_bf16 v[118:121], v[194:197], v[222:225], v[118:121]
	v_mfma_f32_16x16x32_bf16 v[98:101], v[198:201], v[222:225], v[98:101]
	v_mfma_f32_16x16x32_bf16 v[74:77], v[202:205], v[222:225], v[74:77]
	s_waitcnt lgkmcnt(6)
	v_mfma_f32_16x16x32_bf16 v[110:113], v[178:181], v[226:229], v[110:113]
	v_mfma_f32_16x16x32_bf16 v[102:105], v[194:197], v[226:229], v[102:105]
	v_mfma_f32_16x16x32_bf16 v[82:85], v[198:201], v[226:229], v[82:85]
	v_mfma_f32_16x16x32_bf16 v[62:65], v[202:205], v[226:229], v[62:65]
	s_waitcnt lgkmcnt(5)
	v_mfma_f32_16x16x32_bf16 v[94:97], v[178:181], v[230:233], v[94:97]
	v_mfma_f32_16x16x32_bf16 v[86:89], v[194:197], v[230:233], v[86:89]
	v_mfma_f32_16x16x32_bf16 v[70:73], v[198:201], v[230:233], v[70:73]
	v_mfma_f32_16x16x32_bf16 v[54:57], v[202:205], v[230:233], v[54:57]
	s_waitcnt lgkmcnt(4)
	v_mfma_f32_16x16x32_bf16 v[78:81], v[178:181], v[234:237], v[78:81]
	v_mfma_f32_16x16x32_bf16 v[66:69], v[194:197], v[234:237], v[66:69]
	v_mfma_f32_16x16x32_bf16 v[58:61], v[198:201], v[234:237], v[58:61]
	v_mfma_f32_16x16x32_bf16 v[50:53], v[202:205], v[234:237], v[50:53]
	s_waitcnt lgkmcnt(0)
	s_barrier
	s_add_i32 s20, s20, 1
	s_add_i32 s18, s18, 2
	v_add_u32_e32 v182, s19, v191
	v_add_u32_e32 v238, s19, v192
	ds_read_b128 v[178:181], v182 offset:32768
	ds_read_b128 v[194:197], v182 offset:34816
	ds_read_b128 v[198:201], v182 offset:36864
	ds_read_b128 v[202:205], v182 offset:38912
	ds_read_b128 v[206:209], v238
	ds_read_b128 v[210:213], v238 offset:2048
	ds_read_b128 v[214:217], v238 offset:4096
	ds_read_b128 v[218:221], v238 offset:6144
	ds_read_b128 v[222:225], v238 offset:8192
	ds_read_b128 v[226:229], v238 offset:10240
	ds_read_b128 v[230:233], v238 offset:12288
	ds_read_b128 v[234:237], v238 offset:14336
	s_min_u32 s21, s20, 29
	s_xor_b32 s19, s19, 0x10000
	v_add_u32_e32 v239, s19, v189
	s_waitcnt lgkmcnt(0)
	s_add_i32 s21, s21, 2
	s_barrier
	s_waitcnt lgkmcnt(11)
	v_mfma_f32_16x16x32_bf16 v[174:177], v[178:181], v[206:209], v[174:177]
	s_lshl_b32 s22, s21, 1
	s_and_b32 s22, s22, 0x60
	s_add_i32 s22, s22, s12
	s_lshl_b32 s22, s22, 6
	v_mfma_f32_16x16x32_bf16 v[170:173], v[194:197], v[206:209], v[170:173]
	s_and_b32 s22, s22, 0x3f00
	s_or_b32 s22, s22, s13
	s_add_i32 s26, s21, s27
	s_lshl_b32 s23, s26, 23
	s_lshl_b32 s22, s22, 9
	v_mfma_f32_16x16x32_bf16 v[158:161], v[198:201], v[206:209], v[158:161]
	s_and_b32 s23, s23, 0x7000000
	s_or_b32 s22, s22, s23
	s_lshl_b32 s23, s21, 8
	s_and_b32 s23, s23, 0x100
	s_or_b32 s22, s22, s23
	s_or_b32 s23, s22, 0x4000
	v_mfma_f32_16x16x32_bf16 v[142:145], v[202:205], v[206:209], v[142:145]
	s_waitcnt lgkmcnt(10)
	v_mfma_f32_16x16x32_bf16 v[166:169], v[178:181], v[210:213], v[166:169]
	v_mfma_f32_16x16x32_bf16 v[162:165], v[194:197], v[210:213], v[162:165]
	v_mfma_f32_16x16x32_bf16 v[146:149], v[198:201], v[210:213], v[146:149]
	s_or_b32 s23, s22, 0x8000
	v_mfma_f32_16x16x32_bf16 v[122:125], v[202:205], v[210:213], v[122:125]
	s_waitcnt lgkmcnt(9)
	v_mfma_f32_16x16x32_bf16 v[154:157], v[178:181], v[214:217], v[154:157]
	v_mfma_f32_16x16x32_bf16 v[150:153], v[194:197], v[214:217], v[150:153]
	v_mfma_f32_16x16x32_bf16 v[130:133], v[198:201], v[214:217], v[130:133]
	s_or_b32 s23, s22, 0xc000
	v_mfma_f32_16x16x32_bf16 v[106:109], v[202:205], v[214:217], v[106:109]
	s_waitcnt lgkmcnt(8)
	v_mfma_f32_16x16x32_bf16 v[138:141], v[178:181], v[218:221], v[138:141]
	v_mfma_f32_16x16x32_bf16 v[134:137], v[194:197], v[218:221], v[134:137]
	v_mfma_f32_16x16x32_bf16 v[114:117], v[198:201], v[218:221], v[114:117]
	s_or_b32 s23, s22, 0x10000
	v_mfma_f32_16x16x32_bf16 v[90:93], v[202:205], v[218:221], v[90:93]
	s_waitcnt lgkmcnt(7)
	v_mfma_f32_16x16x32_bf16 v[126:129], v[178:181], v[222:225], v[126:129]
	v_mfma_f32_16x16x32_bf16 v[118:121], v[194:197], v[222:225], v[118:121]
	v_mfma_f32_16x16x32_bf16 v[98:101], v[198:201], v[222:225], v[98:101]
	s_or_b32 s23, s22, 0x14000
	v_mfma_f32_16x16x32_bf16 v[74:77], v[202:205], v[222:225], v[74:77]
	s_waitcnt lgkmcnt(6)
	v_mfma_f32_16x16x32_bf16 v[110:113], v[178:181], v[226:229], v[110:113]
	v_mfma_f32_16x16x32_bf16 v[102:105], v[194:197], v[226:229], v[102:105]
	v_mfma_f32_16x16x32_bf16 v[82:85], v[198:201], v[226:229], v[82:85]
	s_or_b32 s23, s22, 0x18000
	s_or_b32 s22, s22, 0x1c000
	v_mfma_f32_16x16x32_bf16 v[62:65], v[202:205], v[226:229], v[62:65]
	s_waitcnt lgkmcnt(5)
	v_mfma_f32_16x16x32_bf16 v[94:97], v[178:181], v[230:233], v[94:97]
	v_mfma_f32_16x16x32_bf16 v[86:89], v[194:197], v[230:233], v[86:89]
	v_mfma_f32_16x16x32_bf16 v[70:73], v[198:201], v[230:233], v[70:73]
	v_mfma_f32_16x16x32_bf16 v[54:57], v[202:205], v[230:233], v[54:57]
	s_waitcnt lgkmcnt(4)
	v_mfma_f32_16x16x32_bf16 v[78:81], v[178:181], v[234:237], v[78:81]
	v_mfma_f32_16x16x32_bf16 v[66:69], v[194:197], v[234:237], v[66:69]
	v_mfma_f32_16x16x32_bf16 v[58:61], v[198:201], v[234:237], v[58:61]
	v_mfma_f32_16x16x32_bf16 v[50:53], v[202:205], v[234:237], v[50:53]
	s_waitcnt lgkmcnt(0)
	s_barrier
	ds_read_b128 v[178:181], v182 offset:33792
	ds_read_b128 v[194:197], v182 offset:35840
	ds_read_b128 v[198:201], v182 offset:37888
	ds_read_b128 v[202:205], v182 offset:39936
	ds_read_b128 v[206:209], v238 offset:1024
	ds_read_b128 v[210:213], v238 offset:3072
	ds_read_b128 v[214:217], v238 offset:5120
	ds_read_b128 v[218:221], v238 offset:7168
	ds_read_b128 v[222:225], v238 offset:9216
	ds_read_b128 v[226:229], v238 offset:11264
	ds_read_b128 v[230:233], v238 offset:13312
	ds_read_b128 v[234:237], v238 offset:15360
	s_waitcnt lgkmcnt(0)
	s_barrier
	s_waitcnt lgkmcnt(11)
	v_mfma_f32_16x16x32_bf16 v[174:177], v[178:181], v[206:209], v[174:177]
	s_lshl_b32 s21, s26, 15
	s_and_b32 s21, s21, 0x78000
	s_or_b32 s21, s21, s14
	s_or_b32 s22, s21, 0x2000
	v_mfma_f32_16x16x32_bf16 v[170:173], v[194:197], v[206:209], v[170:173]
	v_mfma_f32_16x16x32_bf16 v[158:161], v[198:201], v[206:209], v[158:161]
	v_mfma_f32_16x16x32_bf16 v[142:145], v[202:205], v[206:209], v[142:145]
	s_waitcnt lgkmcnt(10)
	v_mfma_f32_16x16x32_bf16 v[166:169], v[178:181], v[210:213], v[166:169]
	v_mfma_f32_16x16x32_bf16 v[162:165], v[194:197], v[210:213], v[162:165]
	v_mfma_f32_16x16x32_bf16 v[146:149], v[198:201], v[210:213], v[146:149]
	v_mfma_f32_16x16x32_bf16 v[122:125], v[202:205], v[210:213], v[122:125]
	s_waitcnt lgkmcnt(9)
	v_mfma_f32_16x16x32_bf16 v[154:157], v[178:181], v[214:217], v[154:157]
	v_mfma_f32_16x16x32_bf16 v[150:153], v[194:197], v[214:217], v[150:153]
	v_mfma_f32_16x16x32_bf16 v[130:133], v[198:201], v[214:217], v[130:133]
	v_mfma_f32_16x16x32_bf16 v[106:109], v[202:205], v[214:217], v[106:109]
	s_waitcnt lgkmcnt(8)
	v_mfma_f32_16x16x32_bf16 v[138:141], v[178:181], v[218:221], v[138:141]
	v_mfma_f32_16x16x32_bf16 v[134:137], v[194:197], v[218:221], v[134:137]
	s_or_b32 s22, s21, 0x4000
	s_or_b32 s21, s21, 0x6000
	v_mfma_f32_16x16x32_bf16 v[114:117], v[198:201], v[218:221], v[114:117]
	v_mfma_f32_16x16x32_bf16 v[90:93], v[202:205], v[218:221], v[90:93]
	s_waitcnt lgkmcnt(7)
	v_mfma_f32_16x16x32_bf16 v[126:129], v[178:181], v[222:225], v[126:129]
	v_mfma_f32_16x16x32_bf16 v[118:121], v[194:197], v[222:225], v[118:121]
	v_mfma_f32_16x16x32_bf16 v[98:101], v[198:201], v[222:225], v[98:101]
	v_mfma_f32_16x16x32_bf16 v[74:77], v[202:205], v[222:225], v[74:77]
	s_waitcnt lgkmcnt(6)
	v_mfma_f32_16x16x32_bf16 v[110:113], v[178:181], v[226:229], v[110:113]
	v_mfma_f32_16x16x32_bf16 v[102:105], v[194:197], v[226:229], v[102:105]
	v_mfma_f32_16x16x32_bf16 v[82:85], v[198:201], v[226:229], v[82:85]
	v_mfma_f32_16x16x32_bf16 v[62:65], v[202:205], v[226:229], v[62:65]
	s_waitcnt lgkmcnt(5)
	v_mfma_f32_16x16x32_bf16 v[94:97], v[178:181], v[230:233], v[94:97]
	v_mfma_f32_16x16x32_bf16 v[86:89], v[194:197], v[230:233], v[86:89]
	v_mfma_f32_16x16x32_bf16 v[70:73], v[198:201], v[230:233], v[70:73]
	v_mfma_f32_16x16x32_bf16 v[54:57], v[202:205], v[230:233], v[54:57]
	s_waitcnt lgkmcnt(4)
	v_mfma_f32_16x16x32_bf16 v[78:81], v[178:181], v[234:237], v[78:81]
	v_mfma_f32_16x16x32_bf16 v[66:69], v[194:197], v[234:237], v[66:69]
	v_mfma_f32_16x16x32_bf16 v[58:61], v[198:201], v[234:237], v[58:61]
	v_mfma_f32_16x16x32_bf16 v[50:53], v[202:205], v[234:237], v[50:53]
	s_and_b32 s21, s18, 32
	s_add_i32 s21, s21, s12
	s_lshl_b32 s21, s21, 6
	s_and_b32 s21, s21, 0x3f00
	v_add_lshl_u32 v182, v193, s21, 9
	v_lshl_add_u64 v[206:207], v[184:185], 0, v[182:183]
	v_add_co_u32_e32 v208, vcc, s8, v206
	s_nop 1
	v_addc_co_u32_e32 v209, vcc, 0, v207, vcc
	v_add_co_u32_e32 v210, vcc, s15, v206
	s_nop 1
	v_addc_co_u32_e32 v211, vcc, 0, v207, vcc
	v_add_co_u32_e32 v212, vcc, s9, v206
	s_nop 1
	v_addc_co_u32_e32 v213, vcc, 0, v207, vcc
	v_add_co_u32_e32 v214, vcc, s16, v206
	s_nop 1
	v_addc_co_u32_e32 v215, vcc, 0, v207, vcc
	v_add_co_u32_e32 v216, vcc, s10, v206
	s_nop 1
	v_addc_co_u32_e32 v217, vcc, 0, v207, vcc
	v_add_co_u32_e32 v218, vcc, s17, v206
	s_nop 1
	v_addc_co_u32_e32 v219, vcc, 0, v207, vcc
	v_add_co_u32_e32 v220, vcc, s11, v206
	s_nop 1
	v_addc_co_u32_e32 v221, vcc, 0, v207, vcc
	global_store_dwordx4 v[206:207], v[174:177], off
	global_store_dwordx4 v[206:207], v[170:173], off offset:64
	global_store_dwordx4 v[206:207], v[158:161], off offset:128
	global_store_dwordx4 v[206:207], v[142:145], off offset:192
	global_store_dwordx4 v[208:209], v[166:169], off
	global_store_dwordx4 v[208:209], v[162:165], off offset:64
	global_store_dwordx4 v[208:209], v[146:149], off offset:128
	global_store_dwordx4 v[208:209], v[122:125], off offset:192
	global_store_dwordx4 v[210:211], v[154:157], off
	global_store_dwordx4 v[210:211], v[150:153], off offset:64
	global_store_dwordx4 v[210:211], v[130:133], off offset:128
	global_store_dwordx4 v[210:211], v[106:109], off offset:192
	global_store_dwordx4 v[212:213], v[138:141], off
	global_store_dwordx4 v[212:213], v[134:137], off offset:64
	global_store_dwordx4 v[212:213], v[114:117], off offset:128
	global_store_dwordx4 v[212:213], v[90:93], off offset:192
	global_store_dwordx4 v[214:215], v[126:129], off
	global_store_dwordx4 v[214:215], v[118:121], off offset:64
	global_store_dwordx4 v[214:215], v[98:101], off offset:128
	global_store_dwordx4 v[214:215], v[74:77], off offset:192
	global_store_dwordx4 v[216:217], v[110:113], off
	global_store_dwordx4 v[216:217], v[102:105], off offset:64
	global_store_dwordx4 v[216:217], v[82:85], off offset:128
	global_store_dwordx4 v[216:217], v[62:65], off offset:192
	global_store_dwordx4 v[218:219], v[94:97], off
	global_store_dwordx4 v[218:219], v[86:89], off offset:64
	global_store_dwordx4 v[218:219], v[70:73], off offset:128
	global_store_dwordx4 v[218:219], v[54:57], off offset:192
	global_store_dwordx4 v[220:221], v[78:81], off
	global_store_dwordx4 v[220:221], v[66:69], off offset:64
	global_store_dwordx4 v[220:221], v[58:61], off offset:128
	global_store_dwordx4 v[220:221], v[50:53], off offset:192
	s_waitcnt lgkmcnt(0)
	s_barrier
	s_branch .LBB1_6
.Lfirst:
	v_add_u32_e32 v182, s19, v191
	v_add_u32_e32 v238, s19, v192
	ds_read_b128 v[178:181], v182 offset:32768
	ds_read_b128 v[194:197], v182 offset:34816
	ds_read_b128 v[198:201], v182 offset:36864
	ds_read_b128 v[202:205], v182 offset:38912
	ds_read_b128 v[206:209], v238
	ds_read_b128 v[210:213], v238 offset:2048
	ds_read_b128 v[214:217], v238 offset:4096
	ds_read_b128 v[218:221], v238 offset:6144
	ds_read_b128 v[222:225], v238 offset:8192
	ds_read_b128 v[226:229], v238 offset:10240
	ds_read_b128 v[230:233], v238 offset:12288
	ds_read_b128 v[234:237], v238 offset:14336
	s_min_u32 s21, s20, 29
	s_xor_b32 s19, s19, 0x10000
	v_add_u32_e32 v239, s19, v189
	s_waitcnt vmcnt(11)
	v_cvt_pk_bf16_f32 v13, v12, v13
	v_cvt_pk_bf16_f32 v12, v10, v11
	s_waitcnt vmcnt(10)
	v_cvt_pk_bf16_f32 v11, v20, v21
	v_cvt_pk_bf16_f32 v10, v18, v19
	ds_write2st64_b64 v239, v[12:13], v[10:11] offset1:8
	s_waitcnt vmcnt(9)
	v_cvt_pk_bf16_f32 v11, v24, v25
	v_cvt_pk_bf16_f32 v10, v22, v23
	s_waitcnt vmcnt(8)
	v_cvt_pk_bf16_f32 v13, v32, v33
	v_cvt_pk_bf16_f32 v12, v30, v31
	ds_write2st64_b64 v239, v[10:11], v[12:13] offset0:16 offset1:24
	s_waitcnt vmcnt(7)
	v_cvt_pk_bf16_f32 v11, v36, v37
	v_cvt_pk_bf16_f32 v10, v34, v35
	s_waitcnt vmcnt(6)
	v_cvt_pk_bf16_f32 v13, v40, v41
	v_cvt_pk_bf16_f32 v12, v38, v39
	ds_write2st64_b64 v239, v[10:11], v[12:13] offset0:32 offset1:40
	s_waitcnt vmcnt(5)
	v_cvt_pk_bf16_f32 v11, v44, v45
	v_cvt_pk_bf16_f32 v10, v42, v43
	s_waitcnt vmcnt(4)
	v_cvt_pk_bf16_f32 v13, v48, v49
	v_cvt_pk_bf16_f32 v12, v46, v47
	ds_write2st64_b64 v239, v[10:11], v[12:13] offset0:48 offset1:56
	s_waitcnt lgkmcnt(0)
	s_add_i32 s21, s21, 2
	s_barrier
	s_waitcnt lgkmcnt(11)
	v_mfma_f32_16x16x32_bf16 v[174:177], v[178:181], v[206:209], v[240:243]
	s_lshl_b32 s22, s21, 1
	s_and_b32 s22, s22, 0x60
	s_add_i32 s22, s22, s12
	s_lshl_b32 s22, s22, 6
	v_mfma_f32_16x16x32_bf16 v[170:173], v[194:197], v[206:209], v[244:247]
	s_and_b32 s22, s22, 0x3f00
	s_or_b32 s22, s22, s13
	s_add_i32 s26, s21, s27
	s_lshl_b32 s23, s26, 23
	s_lshl_b32 s22, s22, 9
	v_mfma_f32_16x16x32_bf16 v[158:161], v[198:201], v[206:209], v[248:251]
	s_and_b32 s23, s23, 0x7000000
	s_or_b32 s22, s22, s23
	s_lshl_b32 s23, s21, 8
	s_and_b32 s23, s23, 0x100
	s_or_b32 s22, s22, s23
	s_or_b32 s23, s22, 0x4000
	buffer_load_dwordx4 v[10:13], v1, s[4:7], s22 offen sc0 nt
	v_mfma_f32_16x16x32_bf16 v[142:145], v[202:205], v[206:209], v[252:255]
	s_waitcnt lgkmcnt(10)
	v_mfma_f32_16x16x32_bf16 v[166:169], v[178:181], v[210:213], v[240:243]
	v_mfma_f32_16x16x32_bf16 v[162:165], v[194:197], v[210:213], v[244:247]
	v_mfma_f32_16x16x32_bf16 v[146:149], v[198:201], v[210:213], v[248:251]
	buffer_load_dwordx4 v[18:21], v1, s[4:7], s23 offen sc0 nt
	s_or_b32 s23, s22, 0x8000
	v_mfma_f32_16x16x32_bf16 v[122:125], v[202:205], v[210:213], v[252:255]
	s_waitcnt lgkmcnt(9)
	v_mfma_f32_16x16x32_bf16 v[154:157], v[178:181], v[214:217], v[240:243]
	v_mfma_f32_16x16x32_bf16 v[150:153], v[194:197], v[214:217], v[244:247]
	v_mfma_f32_16x16x32_bf16 v[130:133], v[198:201], v[214:217], v[248:251]
	buffer_load_dwordx4 v[22:25], v1, s[4:7], s23 offen sc0 nt
	s_or_b32 s23, s22, 0xc000
	v_mfma_f32_16x16x32_bf16 v[106:109], v[202:205], v[214:217], v[252:255]
	s_waitcnt lgkmcnt(8)
	v_mfma_f32_16x16x32_bf16 v[138:141], v[178:181], v[218:221], v[240:243]
	v_mfma_f32_16x16x32_bf16 v[134:137], v[194:197], v[218:221], v[244:247]
	v_mfma_f32_16x16x32_bf16 v[114:117], v[198:201], v[218:221], v[248:251]
	buffer_load_dwordx4 v[30:33], v1, s[4:7], s23 offen sc0 nt
	s_or_b32 s23, s22, 0x10000
	v_mfma_f32_16x16x32_bf16 v[90:93], v[202:205], v[218:221], v[252:255]
	s_waitcnt lgkmcnt(7)
	v_mfma_f32_16x16x32_bf16 v[126:129], v[178:181], v[222:225], v[240:243]
	v_mfma_f32_16x16x32_bf16 v[118:121], v[194:197], v[222:225], v[244:247]
	v_mfma_f32_16x16x32_bf16 v[98:101], v[198:201], v[222:225], v[248:251]
	buffer_load_dwordx4 v[34:37], v1, s[4:7], s23 offen sc0 nt
	s_or_b32 s23, s22, 0x14000
	v_mfma_f32_16x16x32_bf16 v[74:77], v[202:205], v[222:225], v[252:255]
	s_waitcnt lgkmcnt(6)
	v_mfma_f32_16x16x32_bf16 v[110:113], v[178:181], v[226:229], v[240:243]
	v_mfma_f32_16x16x32_bf16 v[102:105], v[194:197], v[226:229], v[244:247]
	v_mfma_f32_16x16x32_bf16 v[82:85], v[198:201], v[226:229], v[248:251]
	buffer_load_dwordx4 v[38:41], v1, s[4:7], s23 offen sc0 nt
	s_or_b32 s23, s22, 0x18000
	s_or_b32 s22, s22, 0x1c000
	v_mfma_f32_16x16x32_bf16 v[62:65], v[202:205], v[226:229], v[252:255]
	s_waitcnt lgkmcnt(5)
	v_mfma_f32_16x16x32_bf16 v[94:97], v[178:181], v[230:233], v[240:243]
	v_mfma_f32_16x16x32_bf16 v[86:89], v[194:197], v[230:233], v[244:247]
	v_mfma_f32_16x16x32_bf16 v[70:73], v[198:201], v[230:233], v[248:251]
	buffer_load_dwordx4 v[42:45], v1, s[4:7], s23 offen sc0 nt
	v_mfma_f32_16x16x32_bf16 v[54:57], v[202:205], v[230:233], v[252:255]
	s_waitcnt lgkmcnt(4)
	v_mfma_f32_16x16x32_bf16 v[78:81], v[178:181], v[234:237], v[240:243]
	v_mfma_f32_16x16x32_bf16 v[66:69], v[194:197], v[234:237], v[244:247]
	v_mfma_f32_16x16x32_bf16 v[58:61], v[198:201], v[234:237], v[248:251]
	buffer_load_dwordx4 v[46:49], v1, s[4:7], s22 offen sc0 nt
	v_mfma_f32_16x16x32_bf16 v[50:53], v[202:205], v[234:237], v[252:255]
	s_waitcnt lgkmcnt(0)
	s_barrier
	ds_read_b128 v[178:181], v182 offset:33792
	ds_read_b128 v[194:197], v182 offset:35840
	ds_read_b128 v[198:201], v182 offset:37888
	ds_read_b128 v[202:205], v182 offset:39936
	ds_read_b128 v[206:209], v238 offset:1024
	ds_read_b128 v[210:213], v238 offset:3072
	ds_read_b128 v[214:217], v238 offset:5120
	ds_read_b128 v[218:221], v238 offset:7168
	ds_read_b128 v[222:225], v238 offset:9216
	ds_read_b128 v[226:229], v238 offset:11264
	ds_read_b128 v[230:233], v238 offset:13312
	ds_read_b128 v[234:237], v238 offset:15360
	v_add_u32_e32 v182, s19, v190
	s_waitcnt vmcnt(11)
	ds_write_b128 v182, v[2:5] offset:32768
	s_waitcnt vmcnt(10)
	ds_write_b128 v182, v[6:9] offset:40960
	s_waitcnt vmcnt(9)
	ds_write_b128 v182, v[14:17] offset:49152
	s_waitcnt vmcnt(8)
	ds_write_b128 v182, v[26:29] offset:57344
	s_waitcnt lgkmcnt(0)
	s_barrier
	s_waitcnt lgkmcnt(11)
	v_mfma_f32_16x16x32_bf16 v[174:177], v[178:181], v[206:209], v[174:177]
	s_lshl_b32 s21, s26, 15
	s_and_b32 s21, s21, 0x78000
	s_or_b32 s21, s21, s14
	s_or_b32 s22, s21, 0x2000
	v_mfma_f32_16x16x32_bf16 v[170:173], v[194:197], v[206:209], v[170:173]
	v_mfma_f32_16x16x32_bf16 v[158:161], v[198:201], v[206:209], v[158:161]
	v_mfma_f32_16x16x32_bf16 v[142:145], v[202:205], v[206:209], v[142:145]
	s_waitcnt lgkmcnt(10)
	v_mfma_f32_16x16x32_bf16 v[166:169], v[178:181], v[210:213], v[166:169]
	v_mfma_f32_16x16x32_bf16 v[162:165], v[194:197], v[210:213], v[162:165]
	buffer_load_dwordx4 v[2:5], v188, s[0:3], s21 offen sc1
	v_mfma_f32_16x16x32_bf16 v[146:149], v[198:201], v[210:213], v[146:149]
	v_mfma_f32_16x16x32_bf16 v[122:125], v[202:205], v[210:213], v[122:125]
	s_waitcnt lgkmcnt(9)
	v_mfma_f32_16x16x32_bf16 v[154:157], v[178:181], v[214:217], v[154:157]
	v_mfma_f32_16x16x32_bf16 v[150:153], v[194:197], v[214:217], v[150:153]
	v_mfma_f32_16x16x32_bf16 v[130:133], v[198:201], v[214:217], v[130:133]
	v_mfma_f32_16x16x32_bf16 v[106:109], v[202:205], v[214:217], v[106:109]
	s_waitcnt lgkmcnt(8)
	v_mfma_f32_16x16x32_bf16 v[138:141], v[178:181], v[218:221], v[138:141]
	v_mfma_f32_16x16x32_bf16 v[134:137], v[194:197], v[218:221], v[134:137]
	buffer_load_dwordx4 v[6:9], v188, s[0:3], s22 offen sc1
	s_or_b32 s22, s21, 0x4000
	s_or_b32 s21, s21, 0x6000
	v_mfma_f32_16x16x32_bf16 v[114:117], v[198:201], v[218:221], v[114:117]
	v_mfma_f32_16x16x32_bf16 v[90:93], v[202:205], v[218:221], v[90:93]
	s_waitcnt lgkmcnt(7)
	v_mfma_f32_16x16x32_bf16 v[126:129], v[178:181], v[222:225], v[126:129]
	v_mfma_f32_16x16x32_bf16 v[118:121], v[194:197], v[222:225], v[118:121]
	v_mfma_f32_16x16x32_bf16 v[98:101], v[198:201], v[222:225], v[98:101]
	v_mfma_f32_16x16x32_bf16 v[74:77], v[202:205], v[222:225], v[74:77]
	s_waitcnt lgkmcnt(6)
	v_mfma_f32_16x16x32_bf16 v[110:113], v[178:181], v[226:229], v[110:113]
	v_mfma_f32_16x16x32_bf16 v[102:105], v[194:197], v[226:229], v[102:105]
	buffer_load_dwordx4 v[14:17], v188, s[0:3], s22 offen sc1
	v_mfma_f32_16x16x32_bf16 v[82:85], v[198:201], v[226:229], v[82:85]
	v_mfma_f32_16x16x32_bf16 v[62:65], v[202:205], v[226:229], v[62:65]
	s_waitcnt lgkmcnt(5)
	v_mfma_f32_16x16x32_bf16 v[94:97], v[178:181], v[230:233], v[94:97]
	v_mfma_f32_16x16x32_bf16 v[86:89], v[194:197], v[230:233], v[86:89]
	v_mfma_f32_16x16x32_bf16 v[70:73], v[198:201], v[230:233], v[70:73]
	v_mfma_f32_16x16x32_bf16 v[54:57], v[202:205], v[230:233], v[54:57]
	s_waitcnt lgkmcnt(4)
	v_mfma_f32_16x16x32_bf16 v[78:81], v[178:181], v[234:237], v[78:81]
	v_mfma_f32_16x16x32_bf16 v[66:69], v[194:197], v[234:237], v[66:69]
	buffer_load_dwordx4 v[26:29], v188, s[0:3], s21 offen sc1
	v_mfma_f32_16x16x32_bf16 v[58:61], v[198:201], v[234:237], v[58:61]
	v_mfma_f32_16x16x32_bf16 v[50:53], v[202:205], v[234:237], v[50:53]
	s_branch .LBB1_3
